# speedup vs baseline: 1.1338x; 1.0095x over previous
.LBB0_3:
	s_load_dwordx8 s[20:27], s[0:1], 0x68
	v_and_b32_e32 v2, 31, v0
	s_lshr_b32 s3, s2, 3
	s_and_b32 s30, s2, 7
	v_cmp_gt_u32_e64 s[10:11], 21, v2
	s_mul_i32 s30, s30, 0x30000
	v_lshrrev_b32_e32 v6, 5, v0
	v_cndmask_b32_e64 v1, 0, v2, s[10:11]
	s_cmpk_gt_u32 s2, 0x41f
	s_cbranch_scc0 .LBB0_11
	s_cmpk_gt_u32 s2, 0x45f
	s_cbranch_scc0 .LBB0_8
	s_load_dwordx2 s[28:29], s[0:1], 0x60
	s_load_dwordx2 s[18:19], s[0:1], 0x48
	s_load_dwordx2 s[8:9], s[0:1], 0x38
	s_load_dwordx2 s[32:33], s[0:1], 0x40
	s_load_dwordx4 s[36:39], s[0:1], 0x50
	v_lshrrev_b32_e32 v3, 2, v2
	v_and_b32_e32 v2, 28, v2
	v_and_b32_e32 v7, 3, v0
	v_and_b32_e32 v51, 7, v0
	v_lshlrev_b32_e32 v51, 2, v51
	s_waitcnt lgkmcnt(0)
	global_load_dword v52, v51, s[28:29]
	global_load_dword v53, v51, s[32:33]
	global_load_dword v54, v51, s[38:39]
	global_load_dword v55, v51, s[36:37]
	global_load_dword v51, v51, s[18:19]
	global_load_dword v22, v2, s[18:19]
	global_load_dword v23, v2, s[28:29]
	v_cmp_lt_u32_e32 vcc, 31, v0
	v_mul_u32_u24_e32 v24, 27, v3
	v_sub_u32_e32 v27, 2, v7
	v_cndmask_b32_e64 v2, 0, 1, vcc
	v_sub_co_u32_e32 v26, vcc, 1, v7
	v_max_i32_e32 v8, 0, v26
	v_lshl_add_u32 v8, v8, 3, v8
	v_sub_u32_e32 v16, 4, v7
	v_add_lshl_u32 v4, v24, v2, 2
	v_mov_b32_e32 v5, 0
	v_ashrrev_i32_e32 v9, 31, v8
	v_max_i32_e32 v12, 0, v27
	v_min_u32_e32 v16, 2, v16
	v_lshl_add_u64 v[2:3], s[8:9], 0, v[4:5]
	v_lshlrev_b64 v[8:9], 2, v[8:9]
	v_mul_u32_u24_e32 v12, 9, v12
	v_mul_u32_u24_e32 v16, 9, v16
	v_lshl_add_u64 v[10:11], v[2:3], 0, v[8:9]
	v_lshlrev_b32_e32 v12, 2, v12
	v_mov_b32_e32 v13, v5
	v_lshlrev_b32_e32 v16, 2, v16
	v_mov_b32_e32 v17, v5
	global_load_dword v25, v4, s[8:9]
	v_lshl_add_u64 v[14:15], v[2:3], 0, v[12:13]
	v_lshl_add_u64 v[18:19], v[2:3], 0, v[16:17]
	global_load_dword v28, v[10:11], off
	global_load_dword v29, v[14:15], off
	global_load_dword v30, v[18:19], off
	v_bitop3_b32 v10, v0, 3, v0 bitop3:0xc
	v_min_u32_e32 v10, 2, v10
	v_mul_u32_u24_e32 v10, 9, v10
	v_lshlrev_b32_e32 v10, 2, v10
	v_mov_b32_e32 v11, v5
	v_lshl_add_u64 v[2:3], v[2:3], 0, v[10:11]
	v_cmp_gt_u32_e64 s[4:5], 32, v0
	global_load_dword v31, v[2:3], off
	global_load_dword v32, v4, s[8:9] offset:72
	v_cndmask_b32_e64 v2, 4, 3, s[4:5]
	v_add_lshl_u32 v4, v2, v24, 2
	v_lshl_add_u64 v[2:3], s[8:9], 0, v[4:5]
	v_lshl_add_u64 v[14:15], v[2:3], 0, v[8:9]
	global_load_dword v33, v4, s[8:9]
	global_load_dword v34, v[14:15], off
	v_lshl_add_u64 v[14:15], v[2:3], 0, v[12:13]
	v_lshl_add_u64 v[18:19], v[2:3], 0, v[10:11]
	v_lshl_add_u64 v[2:3], v[2:3], 0, v[16:17]
	global_load_dword v35, v[14:15], off
	global_load_dword v36, v[18:19], off
	global_load_dword v37, v[2:3], off
	global_load_dword v38, v4, s[8:9] offset:72
	v_cndmask_b32_e64 v2, 8, 7, s[4:5]
	v_add_lshl_u32 v4, v2, v24, 2
	v_lshl_add_u64 v[2:3], s[8:9], 0, v[4:5]
	v_lshl_add_u64 v[14:15], v[2:3], 0, v[8:9]
	v_lshl_add_u64 v[18:19], v[2:3], 0, v[12:13]
	v_lshl_add_u64 v[20:21], v[2:3], 0, v[10:11]
	v_lshl_add_u64 v[2:3], v[2:3], 0, v[16:17]
	global_load_dword v39, v4, s[8:9]
	global_load_dword v40, v[14:15], off
	global_load_dword v41, v[18:19], off
	global_load_dword v42, v[20:21], off
	global_load_dword v43, v[2:3], off
	global_load_dword v44, v4, s[8:9] offset:72
	v_cndmask_b32_e64 v2, 5, 2, s[4:5]
	v_add_lshl_u32 v4, v2, v24, 2
	v_lshl_add_u64 v[2:3], s[8:9], 0, v[4:5]
	v_lshl_add_u64 v[14:15], v[2:3], 0, v[8:9]
	v_lshl_add_u64 v[18:19], v[2:3], 0, v[12:13]
	v_lshl_add_u64 v[20:21], v[2:3], 0, v[10:11]
	v_lshl_add_u64 v[2:3], v[2:3], 0, v[16:17]
	global_load_dword v45, v[14:15], off
	global_load_dword v46, v[18:19], off
	global_load_dword v47, v[20:21], off
	global_load_dword v48, v[2:3], off
	global_load_dword v49, v4, s[8:9]
	global_load_dword v50, v4, s[8:9] offset:72
	v_cndmask_b32_e64 v2, 8, 6, s[4:5]
	v_add_lshl_u32 v4, v2, v24, 2
	s_mov_b32 s31, 0x800000
	v_lshl_add_u64 v[2:3], s[8:9], 0, v[4:5]
	v_lshl_add_u64 v[8:9], v[2:3], 0, v[8:9]
	v_lshl_add_u64 v[12:13], v[2:3], 0, v[12:13]
	v_lshl_add_u64 v[10:11], v[2:3], 0, v[10:11]
	v_lshl_add_u64 v[2:3], v[2:3], 0, v[16:17]
	v_cmp_gt_u32_e64 s[12:13], 3, v27
	v_cmp_ne_u32_e64 s[14:15], 0, v7
	v_cmp_eq_u32_e64 s[16:17], 3, v7
	s_add_u32 s24, s24, s30
	s_addc_u32 s25, s25, 0
	s_mov_b32 s34, 0xe52632a
	v_writelane_b32 v56, s34, 0
	s_mov_b32 s34, 0x2102e45
	v_writelane_b32 v56, s34, 1
	s_mov_b32 s34, 0x1f202f6f
	v_writelane_b32 v56, s34, 2
	s_mov_b32 s34, 0x142d0a56
	v_writelane_b32 v56, s34, 3
	s_mov_b32 s34, 0x2b1c1160
	v_writelane_b32 v56, s34, 4
	s_mov_b32 s34, 0x47394854
	v_writelane_b32 v56, s34, 5
	s_mov_b32 s34, 0x12071303
	v_writelane_b32 v56, s34, 6
	s_mov_b32 s34, 0x15746465
	v_writelane_b32 v56, s34, 7
	s_mov_b32 s34, 0x2b5a3e22
	v_writelane_b32 v56, s34, 8
	s_mov_b32 s34, 0x34176831
	v_writelane_b32 v56, s34, 9
	s_mov_b32 s34, 0x50354d33
	v_writelane_b32 v56, s34, 10
	s_mov_b32 s34, 0x1b43114f
	v_writelane_b32 v56, s34, 11
	s_mov_b32 s34, 0x3d66413c
	v_writelane_b32 v56, s34, 12
	s_mov_b32 s34, 0x9235c30
	v_writelane_b32 v56, s34, 13
	s_mov_b32 s34, 0x40695d59
	v_writelane_b32 v56, s34, 14
	s_mov_b32 s34, 0x5e361a4e
	v_writelane_b32 v56, s34, 15
	s_mov_b32 s34, 0x1441d
	v_writelane_b32 v56, s34, 16
	s_mov_b32 s34, 0x46625370
	v_writelane_b32 v56, s34, 17
	s_mov_b32 s34, 0x572c1e3b
	v_writelane_b32 v56, s34, 18
	s_mov_b32 s34, 0x72054b4a
	v_writelane_b32 v56, s34, 19
	s_mov_b32 s34, 0xf37616e
	v_writelane_b32 v56, s34, 20
	s_mov_b32 s34, 0x4376171
	v_writelane_b32 v56, s34, 21
	s_mov_b32 s34, 0x49373821
	v_writelane_b32 v56, s34, 22
	s_mov_b32 s34, 0x4c735516
	v_writelane_b32 v56, s34, 23
	s_mov_b32 s34, 0x25763a77
	v_writelane_b32 v56, s34, 24
	s_mov_b32 s34, 0x266a5827
	v_writelane_b32 v56, s34, 25
	s_mov_b32 s34, 0x190b676c
	v_writelane_b32 v56, s34, 26
	s_mov_b32 s34, 0xd51296d
	v_writelane_b32 v56, s34, 27
	s_mov_b32 s34, 0x8067524
	v_writelane_b32 v56, s34, 28
	s_mov_b32 s34, 0x323f4418
	v_writelane_b32 v56, s34, 29
	s_mov_b32 s34, 0x5b780c42
	v_writelane_b32 v56, s34, 30
	s_mov_b32 s34, 0x6b285f1d
	v_writelane_b32 v56, s34, 31
	s_mov_b32 s34, 0x38587000
	v_writelane_b32 v57, s34, 0
	s_mov_b32 s34, 0xa878
	v_writelane_b32 v58, s34, 0
	s_mov_b32 s34, 0x80482830
	v_writelane_b32 v57, s34, 1
	s_mov_b32 s34, 0xa068
	v_writelane_b32 v58, s34, 1
	s_mov_b32 s34, 0x59790191
	v_writelane_b32 v57, s34, 2
	s_mov_b32 s34, 0x3971
	v_writelane_b32 v58, s34, 2
	s_mov_b32 s34, 0x9949515a
	v_writelane_b32 v57, s34, 3
	s_mov_b32 s34, 0x2969
	v_writelane_b32 v58, s34, 3
	s_mov_b32 s34, 0x222422a
	v_writelane_b32 v57, s34, 4
	s_mov_b32 s34, 0x3a72
	v_writelane_b32 v58, s34, 4
	s_mov_b32 s34, 0x329a1a03
	v_writelane_b32 v57, s34, 5
	s_mov_b32 s34, 0x8a6a
	v_writelane_b32 v58, s34, 5
	s_mov_b32 s34, 0x5b23934b
	v_writelane_b32 v57, s34, 6
	s_mov_b32 s34, 0x3b73
	v_writelane_b32 v58, s34, 6
	s_mov_b32 s34, 0x83541374
	v_writelane_b32 v57, s34, 7
	s_mov_b32 s34, 0x336b
	v_writelane_b32 v58, s34, 7
	s_mov_b32 s34, 0x3c1c2434
	v_writelane_b32 v57, s34, 8
	s_mov_b32 s34, 0x48c
	v_writelane_b32 v58, s34, 8
	s_mov_b32 s34, 0x4c1da455
	v_writelane_b32 v57, s34, 9
	s_mov_b32 s34, 0x449c
	v_writelane_b32 v58, s34, 9
	s_mov_b32 s34, 0x8d25052d
	v_writelane_b32 v57, s34, 10
	s_mov_b32 s34, 0x9d5d
	v_writelane_b32 v58, s34, 10
	s_mov_b32 s34, 0x761e4556
	v_writelane_b32 v57, s34, 11
	s_mov_b32 s34, 0x3565
	v_writelane_b32 v58, s34, 11
	s_mov_b32 s34, 0x46368e6e
	v_writelane_b32 v57, s34, 12
	s_mov_b32 s34, 0x63e
	v_writelane_b32 v58, s34, 12
	s_mov_b32 s34, 0x5f579e77
	v_writelane_b32 v57, s34, 13
	s_mov_b32 s34, 0x2ea6
	v_writelane_b32 v58, s34, 13
	s_mov_b32 s34, 0x174f1f9f
	v_writelane_b32 v57, s34, 14
	s_mov_b32 s34, 0x278f
	v_writelane_b32 v58, s34, 14
	s_mov_b32 s34, 0x38584700
	v_writelane_b32 v57, s34, 15
	s_mov_b32 s34, 0xa897
	v_writelane_b32 v58, s34, 15
	s_mov_b32 s34, 0x90982008
	v_writelane_b32 v57, s34, 16
	s_mov_b32 s34, 0x4060
	v_writelane_b32 v58, s34, 16
	s_mov_b32 s34, 0x411810a1
	v_writelane_b32 v57, s34, 17
	s_mov_b32 s34, 0x5088
	v_writelane_b32 v58, s34, 17
	s_mov_b32 s34, 0x8161197a
	v_writelane_b32 v57, s34, 18
	s_mov_b32 s34, 0x2109
	v_writelane_b32 v58, s34, 18
	s_mov_b32 s34, 0x12314aa2
	v_writelane_b32 v57, s34, 19
	s_mov_b32 s34, 0x1189
	v_writelane_b32 v58, s34, 19
	s_mov_b32 s34, 0x520a430b
	v_writelane_b32 v57, s34, 20
	s_mov_b32 s34, 0x6292
	v_writelane_b32 v58, s34, 20
	s_mov_b32 s34, 0x9b828b53
	v_writelane_b32 v57, s34, 21
	s_mov_b32 s34, 0x2b63
	v_writelane_b32 v58, s34, 21
	s_mov_b32 s34, 0x7c7b5c84
	v_writelane_b32 v57, s34, 22
	s_mov_b32 s34, 0xa31b
	v_writelane_b32 v58, s34, 22
	s_mov_b32 s34, 0x6c0c957d
	v_writelane_b32 v57, s34, 23
	s_mov_b32 s34, 0x942c
	v_writelane_b32 v58, s34, 23
	s_mov_b32 s34, 0x753d85a5
	v_writelane_b32 v57, s34, 24
	s_mov_b32 s34, 0x6414
	v_writelane_b32 v58, s34, 24
	s_mov_b32 s34, 0x5e6d7e26
	v_writelane_b32 v57, s34, 25
	s_mov_b32 s34, 0x4d0d
	v_writelane_b32 v58, s34, 25
	s_mov_b32 s34, 0x8666160f
	v_writelane_b32 v57, s34, 26
	s_mov_b32 s34, 0x9615
	v_writelane_b32 v58, s34, 26
	s_mov_b32 s34, 0x2f7f0787
	v_writelane_b32 v57, s34, 27
	s_mov_b32 s34, 0x4e0e
	v_writelane_b32 v58, s34, 27
	s_mov_b32 s34, 0xa76f2008
	v_writelane_b32 v57, s34, 28
	s_mov_b32 s34, 0x373f
	v_writelane_b32 v58, s34, 28
	s_mov_b32 s34, 0x90982008
	v_writelane_b32 v57, s34, 29
	s_mov_b32 s34, 0x4067
	v_writelane_b32 v58, s34, 29
	s_mov_b32 s34, 0x90982008
	v_writelane_b32 v57, s34, 30
	s_mov_b32 s34, 0x4060
	v_writelane_b32 v58, s34, 30
	s_mov_b32 s34, 0x90982008
	v_writelane_b32 v57, s34, 31
	s_mov_b32 s34, 0x4060
	v_writelane_b32 v58, s34, 31
	s_waitcnt vmcnt(24)
	v_add_f32_e32 v14, 0x3727c5ac, v23
	v_mul_f32_e32 v15, 0x4b800000, v14
	v_cmp_gt_f32_e64 s[6:7], s31, v14
	s_nop 1
	v_cndmask_b32_e64 v14, v14, v15, s[6:7]
	global_load_dword v15, v4, s[8:9]
	global_load_dword v16, v[8:9], off
	global_load_dword v17, v[12:13], off
	global_load_dword v18, v[10:11], off
	global_load_dword v19, v4, s[8:9] offset:72
	global_load_dword v20, v[2:3], off
	v_rsq_f32_e32 v14, v14
	v_cmp_gt_u32_e64 s[8:9], 3, v26
	v_mul_f32_e32 v2, 0x45800000, v14
	v_cndmask_b32_e64 v2, v14, v2, s[6:7]
	v_mul_f32_e32 v12, v22, v2
	v_cmp_eq_u32_e64 s[6:7], 0, v7
	s_waitcnt vmcnt(29)
	v_fma_mixlo_f16 v2, v12, v25, 0
	s_waitcnt vmcnt(28)
	v_fma_mixlo_f16 v3, v12, v28, 0
	v_cndmask_b32_e64 v8, 0, v3, s[8:9]
	s_waitcnt vmcnt(26)
	v_fma_mixlo_f16 v4, v12, v30, 0
	v_fma_mixlo_f16 v3, v12, v29, 0
	v_cndmask_b32_e64 v2, 0, v2, s[6:7]
	v_cndmask_b32_e32 v4, 0, v4, vcc
	v_cndmask_b32_e64 v3, 0, v3, s[12:13]
	v_pack_b32_f16 v2, v2, v8
	v_lshlrev_b32_e32 v8, 4, v0
	s_waitcnt vmcnt(25)
	v_fma_mixlo_f16 v9, v12, v31, 0
	s_waitcnt vmcnt(24)
	v_fma_mixlo_f16 v10, v12, v32, 0
	v_cndmask_b32_e64 v9, 0, v9, s[14:15]
	v_cndmask_b32_e64 v7, 0, v10, s[16:17]
	v_pack_b32_f16 v4, v4, v7
	v_pack_b32_f16 v3, v3, v9
	v_mov_b32_e32 v9, v5
	global_store_dwordx4 v8, v[2:5], s[24:25]
	v_lshl_add_u64 v[10:11], s[24:25], 0, v[8:9]
	s_waitcnt vmcnt(19)
	v_fma_mixlo_f16 v13, v12, v38, 0
	v_fma_mixlo_f16 v3, v12, v34, 0
	v_fma_mixlo_f16 v4, v12, v36, 0
	v_fma_mixlo_f16 v2, v12, v33, 0
	v_cndmask_b32_e64 v7, 0, v3, s[8:9]
	v_fma_mixlo_f16 v3, v12, v35, 0
	v_cndmask_b32_e64 v9, 0, v4, s[14:15]
	v_fma_mixlo_f16 v4, v12, v37, 0
	v_cndmask_b32_e64 v2, 0, v2, s[6:7]
	v_cndmask_b32_e64 v3, 0, v3, s[12:13]
	v_cndmask_b32_e32 v4, 0, v4, vcc
	v_cndmask_b32_e64 v13, 0, v13, s[16:17]
	v_pack_b32_f16 v4, v4, v13
	v_pack_b32_f16 v3, v3, v9
	v_pack_b32_f16 v2, v2, v7
	global_store_dwordx4 v8, v[2:5], s[24:25] offset:1024
	s_waitcnt vmcnt(14)
	v_fma_mixlo_f16 v13, v12, v44, 0
	v_cndmask_b32_e64 v13, 0, v13, s[16:17]
	v_fma_mixlo_f16 v3, v12, v40, 0
	v_fma_mixlo_f16 v4, v12, v42, 0
	v_fma_mixlo_f16 v2, v12, v39, 0
	v_cndmask_b32_e64 v7, 0, v3, s[8:9]
	v_fma_mixlo_f16 v3, v12, v41, 0
	v_cndmask_b32_e64 v9, 0, v4, s[14:15]
	v_fma_mixlo_f16 v4, v12, v43, 0
	v_cndmask_b32_e64 v2, 0, v2, s[6:7]
	v_cndmask_b32_e64 v3, 0, v3, s[12:13]
	v_cndmask_b32_e32 v4, 0, v4, vcc
	v_pack_b32_f16 v4, v4, v13
	v_pack_b32_f16 v3, v3, v9
	v_pack_b32_f16 v2, v2, v7
	global_store_dwordx4 v8, v[2:5], s[24:25] offset:2048
	s_waitcnt vmcnt(9)
	v_fma_mixlo_f16 v13, v12, v50, 0
	v_cndmask_b32_e64 v13, 0, v13, s[16:17]
	v_fma_mixlo_f16 v3, v12, v45, 0
	v_fma_mixlo_f16 v4, v12, v47, 0
	v_fma_mixlo_f16 v2, v12, v49, 0
	v_cndmask_b32_e64 v7, 0, v3, s[8:9]
	v_fma_mixlo_f16 v3, v12, v46, 0
	v_cndmask_b32_e64 v9, 0, v4, s[14:15]
	v_fma_mixlo_f16 v4, v12, v48, 0
	v_cndmask_b32_e64 v2, 0, v2, s[6:7]
	v_cndmask_b32_e64 v3, 0, v3, s[12:13]
	v_cndmask_b32_e32 v4, 0, v4, vcc
	v_pack_b32_f16 v4, v4, v13
	v_pack_b32_f16 v3, v3, v9
	v_pack_b32_f16 v2, v2, v7
	global_store_dwordx4 v8, v[2:5], s[24:25] offset:3072
	s_and_b64 vcc, s[4:5], vcc
	s_nop 0
	v_and_b32_e32 v2, 35, v0
	s_waitcnt vmcnt(9)
	v_fma_mixlo_f16 v3, v12, v15, 0
	v_cmp_eq_u32_e64 s[6:7], 0, v2
	s_waitcnt vmcnt(6)
	v_fma_mixlo_f16 v4, v12, v18, 0
	v_cndmask_b32_e64 v7, 0, v3, s[6:7]
	v_fma_mixlo_f16 v3, v12, v16, 0
	s_and_b64 s[6:7], s[4:5], s[8:9]
	v_cndmask_b32_e64 v8, 0, v3, s[6:7]
	v_fma_mixlo_f16 v3, v12, v17, 0
	s_and_b64 s[6:7], s[4:5], s[12:13]
	v_cndmask_b32_e64 v3, 0, v3, s[6:7]
	s_and_b64 s[6:7], s[4:5], s[14:15]
	v_cndmask_b32_e64 v9, 0, v4, s[6:7]
	s_waitcnt vmcnt(4)
	v_fma_mixlo_f16 v4, v12, v20, 0
	v_cndmask_b32_e32 v4, 0, v4, vcc
	v_fma_mixlo_f16 v12, v12, v19, 0
	v_cmp_eq_u32_e32 vcc, 3, v2
	v_pack_b32_f16 v3, v3, v9
	s_nop 0
	v_cndmask_b32_e32 v2, 0, v12, vcc
	v_pack_b32_f16 v4, v4, v2
	v_pack_b32_f16 v2, v7, v8
	v_add_co_u32_e32 v8, vcc, 0x1000, v10
	s_nop 1
	v_addc_co_u32_e32 v9, vcc, 0, v11, vcc
	v_cmp_gt_u32_e32 vcc, 8, v0
	global_store_dwordx4 v[8:9], v[2:5], off
	s_and_saveexec_b64 s[4:5], vcc
	s_cbranch_execz .LBB0_7
	s_add_u32 s6, s26, s30
	s_addc_u32 s7, s27, 0
	v_add_f32_e32 v2, 0x3727c5ac, v52
	v_mul_f32_e32 v3, 0x4b800000, v2
	v_cmp_gt_f32_e32 vcc, s31, v2
	s_nop 1
	v_cndmask_b32_e32 v2, v2, v3, vcc
	v_rsq_f32_e32 v2, v2
	v_sub_f32_e32 v3, v53, v54
	v_mul_f32_e32 v4, 0x45800000, v2
	v_cndmask_b32_e32 v2, v2, v4, vcc
	v_mul_f32_e32 v2, v51, v2
	v_fmac_f32_e32 v55, v3, v2
	v_lshlrev_b32_e32 v2, 2, v0
	global_store_dword v2, v55, s[6:7]
.LBB0_7:
	s_or_b64 exec, exec, s[4:5]
	s_add_u32 s32, s20, s30
	s_addc_u32 s33, s21, 0
	v_lshlrev_b32_e32 v21, 2, v0
	v_add_u32_e32 v21, 0x21000, v21
	v_cmp_gt_u32_e32 vcc, 32, v0
	s_and_saveexec_b64 s[4:5], vcc
	global_store_dword v21, v56, s[32:33]
	global_store_dword v21, v57, s[32:33] offset:128
	global_store_dword v21, v58, s[32:33] offset:256
	s_or_b64 exec, exec, s[4:5]
	s_mov_b64 s[4:5], 0

	.amdhsa_kernel _Z6k_prepPKfS0_S0_S0_S0_S0_S0_S0_S0_S0_S0_S0_S0_PDv8_DF16_S2_S2_PfS0_
		.amdhsa_group_segment_fixed_size 0
		.amdhsa_private_segment_fixed_size 0
		.amdhsa_kernarg_size 144
		.amdhsa_user_sgpr_count 2
		.amdhsa_user_sgpr_dispatch_ptr 0
		.amdhsa_user_sgpr_queue_ptr 0
		.amdhsa_user_sgpr_kernarg_segment_ptr 1
		.amdhsa_user_sgpr_dispatch_id 0
		.amdhsa_user_sgpr_kernarg_preload_length 0
		.amdhsa_user_sgpr_kernarg_preload_offset 0
		.amdhsa_user_sgpr_private_segment_size 0
		.amdhsa_uses_dynamic_stack 0
		.amdhsa_enable_private_segment 0
		.amdhsa_system_sgpr_workgroup_id_x 1
		.amdhsa_system_sgpr_workgroup_id_y 0
		.amdhsa_system_sgpr_workgroup_id_z 0
		.amdhsa_system_sgpr_workgroup_info 0
		.amdhsa_system_vgpr_workitem_id 0
		.amdhsa_next_free_vgpr 60
		.amdhsa_next_free_sgpr 40
		.amdhsa_accum_offset 60
		.amdhsa_reserve_vcc 1
		.amdhsa_float_round_mode_32 0
		.amdhsa_float_round_mode_16_64 0
		.amdhsa_float_denorm_mode_32 3
		.amdhsa_float_denorm_mode_16_64 3
		.amdhsa_dx10_clamp 1
		.amdhsa_ieee_mode 1
		.amdhsa_fp16_overflow 0
		.amdhsa_tg_split 0
		.amdhsa_exception_fp_ieee_invalid_op 0
		.amdhsa_exception_fp_denorm_src 0
		.amdhsa_exception_fp_ieee_div_zero 0
		.amdhsa_exception_fp_ieee_overflow 0
		.amdhsa_exception_fp_ieee_underflow 0
		.amdhsa_exception_fp_ieee_inexact 0
		.amdhsa_exception_int_div_zero 0
	.end_amdhsa_kernel

amdhsa.kernels:
  - .agpr_count:     0
    .args:
      - .actual_access:  read_only
        .address_space:  global
        .offset:         0
        .size:           8
        .value_kind:     global_buffer
      - .actual_access:  read_only
        .address_space:  global
        .offset:         8
        .size:           8
        .value_kind:     global_buffer
      - .actual_access:  read_only
        .address_space:  global
        .offset:         16
        .size:           8
        .value_kind:     global_buffer
      - .actual_access:  read_only
        .address_space:  global
        .offset:         24
        .size:           8
        .value_kind:     global_buffer
      - .actual_access:  read_only
        .address_space:  global
        .offset:         32
        .size:           8
        .value_kind:     global_buffer
      - .actual_access:  read_only
        .address_space:  global
        .offset:         40
        .size:           8
        .value_kind:     global_buffer
      - .actual_access:  read_only
        .address_space:  global
        .offset:         48
        .size:           8
        .value_kind:     global_buffer
      - .actual_access:  read_only
        .address_space:  global
        .offset:         56
        .size:           8
        .value_kind:     global_buffer
      - .actual_access:  read_only
        .address_space:  global
        .offset:         64
        .size:           8
        .value_kind:     global_buffer
      - .actual_access:  read_only
        .address_space:  global
        .offset:         72
        .size:           8
        .value_kind:     global_buffer
      - .actual_access:  read_only
        .address_space:  global
        .offset:         80
        .size:           8
        .value_kind:     global_buffer
      - .actual_access:  read_only
        .address_space:  global
        .offset:         88
        .size:           8
        .value_kind:     global_buffer
      - .actual_access:  read_only
        .address_space:  global
        .offset:         96
        .size:           8
        .value_kind:     global_buffer
      - .address_space:  global
        .offset:         104
        .size:           8
        .value_kind:     global_buffer
      - .address_space:  global
        .offset:         112
        .size:           8
        .value_kind:     global_buffer
      - .address_space:  global
        .offset:         120
        .size:           8
        .value_kind:     global_buffer
      - .address_space:  global
        .offset:         128
        .size:           8
        .value_kind:     global_buffer
      - .actual_access:  read_only
        .address_space:  global
        .offset:         136
        .size:           8
        .value_kind:     global_buffer
    .group_segment_fixed_size: 0
    .kernarg_segment_align: 8
    .kernarg_segment_size: 144
    .language:       OpenCL C
    .language_version:
      - 2
      - 0
    .max_flat_workgroup_size: 64
    .name:           _Z6k_prepPKfS0_S0_S0_S0_S0_S0_S0_S0_S0_S0_S0_S0_PDv8_DF16_S2_S2_PfS0_
    .private_segment_fixed_size: 0
    .sgpr_count:     46
    .sgpr_spill_count: 0
    .symbol:         _Z6k_prepPKfS0_S0_S0_S0_S0_S0_S0_S0_S0_S0_S0_S0_PDv8_DF16_S2_S2_PfS0_.kd
    .uniform_work_group_size: 1
    .uses_dynamic_stack: false
    .vgpr_count:     60
    .vgpr_spill_count: 0
    .wavefront_size: 64
  - .agpr_count:     0
    .args:
      - .actual_access:  read_only
        .address_space:  global
        .offset:         0
        .size:           8
        .value_kind:     global_buffer
      - .address_space:  global
        .offset:         8
        .size:           8
        .value_kind:     global_buffer
      - .address_space:  global
        .offset:         16
        .size:           8
        .value_kind:     global_buffer
      - .address_space:  global
        .offset:         24
        .size:           8
        .value_kind:     global_buffer
      - .actual_access:  read_only
        .address_space:  global
        .offset:         32
        .size:           8
        .value_kind:     global_buffer
      - .actual_access:  read_only
        .address_space:  global
        .offset:         40
        .size:           8
        .value_kind:     global_buffer
      - .actual_access:  read_only
        .address_space:  global
        .offset:         48
        .size:           8
        .value_kind:     global_buffer
      - .actual_access:  read_only
        .address_space:  global
        .offset:         56
        .size:           8
        .value_kind:     global_buffer
      - .actual_access:  read_only
        .address_space:  global
        .offset:         64
        .size:           8
        .value_kind:     global_buffer
      - .actual_access:  read_only
        .address_space:  global
        .offset:         72
        .size:           8
        .value_kind:     global_buffer
      - .actual_access:  read_only
        .address_space:  global
        .offset:         80
        .size:           8
        .value_kind:     global_buffer
      - .actual_access:  read_only
        .address_space:  global
        .offset:         88
        .size:           8
        .value_kind:     global_buffer
      - .actual_access:  read_only
        .address_space:  global
        .offset:         96
        .size:           8
        .value_kind:     global_buffer
      - .address_space:  global
        .offset:         104
        .size:           8
        .value_kind:     global_buffer
      - .actual_access:  read_only
        .address_space:  global
        .offset:         112
        .size:           8
        .value_kind:     global_buffer
      - .actual_access:  read_only
        .address_space:  global
        .offset:         120
        .size:           8
        .value_kind:     global_buffer
      - .actual_access:  read_only
        .address_space:  global
        .offset:         128
        .size:           8
        .value_kind:     global_buffer
      - .actual_access:  read_only
        .address_space:  global
        .offset:         136
        .size:           8
        .value_kind:     global_buffer
      - .actual_access:  read_only
        .address_space:  global
        .offset:         144
        .size:           8
        .value_kind:     global_buffer
      - .actual_access:  read_only
        .address_space:  global
        .offset:         152
        .size:           8
        .value_kind:     global_buffer
      - .actual_access:  read_only
        .address_space:  global
        .offset:         160
        .size:           8
        .value_kind:     global_buffer
      - .actual_access:  read_only
        .address_space:  global
        .offset:         168
        .size:           8
        .value_kind:     global_buffer
      - .actual_access:  read_only
        .address_space:  global
        .offset:         176
        .size:           8
        .value_kind:     global_buffer
      - .actual_access:  read_only
        .address_space:  global
        .offset:         184
        .size:           8
        .value_kind:     global_buffer
      - .actual_access:  read_only
        .address_space:  global
        .offset:         192
        .size:           8
        .value_kind:     global_buffer
      - .actual_access:  read_only
        .address_space:  global
        .offset:         200
        .size:           8
        .value_kind:     global_buffer
      - .actual_access:  read_only
        .address_space:  global
        .offset:         208
        .size:           8
        .value_kind:     global_buffer
      - .actual_access:  write_only
        .address_space:  global
        .offset:         216
        .size:           8
        .value_kind:     global_buffer
    .group_segment_fixed_size: 78032
    .kernarg_segment_align: 8
    .kernarg_segment_size: 224
    .language:       OpenCL C
    .language_version:
      - 2
      - 0
    .max_flat_workgroup_size: 512
    .name:           _Z6k_mainPKfPKDv8_DF16_S0_S3_S0_S0_S0_S0_S0_S0_S0_S0_S0_S3_S0_S0_S0_S0_S0_S0_S0_S0_S0_S0_S0_S0_S0_Pf
    .private_segment_fixed_size: 0
    .sgpr_count:     78
    .sgpr_spill_count: 0
    .symbol:         _Z6k_mainPKfPKDv8_DF16_S0_S3_S0_S0_S0_S0_S0_S0_S0_S0_S0_S3_S0_S0_S0_S0_S0_S0_S0_S0_S0_S0_S0_S0_S0_Pf.kd
    .uniform_work_group_size: 1
    .uses_dynamic_stack: false
    .vgpr_count:     128
    .vgpr_spill_count: 0
    .wavefront_size: 64
